# v3 + BRANCH and MOE2 epilogue store widening: the two 8-byte fp8 groups of a row exchanged with v_permlane16_swap, one dwordx4 store instead of two dwordx2
# speedup vs baseline: 1.0095x; 1.0024x over previous
.LBB0_1116:
	v_mbcnt_lo_u32_b32 v252, -1, 0
	v_mbcnt_hi_u32_b32 v252, -1, v252
	v_bfe_u32 v252, v252, 4, 1
	v_mul_u32_u24_e32 v252, 0x78, v252
	v_mov_b32_e32 v253, 0
	v_ashrrev_i32_e32 v211, 31, v210
	v_ashrrev_i32_e32 v213, 31, v212
	v_lshl_add_u64 v[2:3], v[210:211], 1, s[24:25]
	v_lshlrev_b64 v[4:5], 12, v[212:213]
	v_lshl_add_u64 v[4:5], v[2:3], 0, v[4:5]
	global_load_dwordx4 v[60:63], v[4:5], off
	global_load_dwordx4 v[214:217], v[4:5], off offset:256
	v_or_b32_e32 v58, 16, v212
	v_or_b32_e32 v56, 32, v212
	v_or_b32_e32 v54, 48, v212
	v_add_u32_e32 v52, 0x80, v212
	v_add_u32_e32 v50, 0x90, v212
	v_add_u32_e32 v48, 0xa0, v212
	v_add_u32_e32 v46, 0xb0, v212
	v_ashrrev_i32_e32 v59, 31, v58
	v_ashrrev_i32_e32 v57, 31, v56
	v_ashrrev_i32_e32 v55, 31, v54
	v_ashrrev_i32_e32 v53, 31, v52
	v_ashrrev_i32_e32 v51, 31, v50
	v_ashrrev_i32_e32 v49, 31, v48
	v_ashrrev_i32_e32 v47, 31, v46
	v_lshlrev_b64 v[212:213], 11, v[212:213]
	v_lshlrev_b64 v[4:5], 12, v[58:59]
	v_lshlrev_b64 v[6:7], 12, v[56:57]
	v_lshlrev_b64 v[8:9], 12, v[54:55]
	v_lshlrev_b64 v[10:11], 12, v[52:53]
	v_lshlrev_b64 v[12:13], 12, v[50:51]
	v_lshlrev_b64 v[14:15], 12, v[48:49]
	v_lshlrev_b64 v[16:17], 12, v[46:47]
	v_lshl_add_u64 v[18:19], s[26:27], 0, v[212:213]
	v_lshl_add_u64 v[4:5], v[2:3], 0, v[4:5]
	v_lshl_add_u64 v[6:7], v[2:3], 0, v[6:7]
	v_lshl_add_u64 v[8:9], v[2:3], 0, v[8:9]
	v_lshl_add_u64 v[10:11], v[2:3], 0, v[10:11]
	v_lshl_add_u64 v[12:13], v[2:3], 0, v[12:13]
	v_lshl_add_u64 v[236:237], v[2:3], 0, v[14:15]
	v_lshl_add_u64 v[2:3], v[2:3], 0, v[16:17]
	v_lshl_add_u64 v[238:239], v[18:19], 0, v[210:211]
	global_load_dwordx4 v[218:221], v[4:5], off
	global_load_dwordx4 v[228:231], v[4:5], off offset:256
	global_load_dwordx4 v[232:235], v[6:7], off
	global_load_dwordx4 v[42:45], v[6:7], off offset:256
	global_load_dwordx4 v[38:41], v[8:9], off
	global_load_dwordx4 v[34:37], v[8:9], off offset:256
	global_load_dwordx4 v[30:33], v[10:11], off
	global_load_dwordx4 v[26:29], v[10:11], off offset:256
	global_load_dwordx4 v[22:25], v[12:13], off
	global_load_dwordx4 v[18:21], v[12:13], off offset:256
	global_load_dwordx4 v[14:17], v[236:237], off
	s_nop 0
	global_load_dwordx4 v[10:13], v[236:237], off offset:256
	global_load_dwordx4 v[6:9], v[2:3], off
	s_nop 0
	global_load_dwordx4 v[2:5], v[2:3], off offset:256
	v_mov_b32_e32 v64, v199
	v_mov_b32_e32 v65, v199
	v_lshlrev_b64 v[58:59], 11, v[58:59]
	v_lshlrev_b64 v[56:57], 11, v[56:57]
	s_waitcnt vmcnt(0)
	v_lshlrev_b32_e32 v201, 16, v60
	v_and_b32_e32 v60, 0xffff0000, v60
	v_lshlrev_b32_e32 v205, 16, v62
	v_and_b32_e32 v62, 0xffff0000, v62
	v_lshlrev_b32_e32 v236, 16, v63
	v_mul_f32_e32 v190, v190, v201
	v_mul_f32_e32 v60, v191, v60
	v_mul_f32_e32 v186, v186, v205
	v_mul_f32_e32 v62, v187, v62
	v_mul_f32_e32 v187, v188, v236
	v_mul_f32_e32 v188, 0x3c800000, v190
	v_mul_f32_e32 v60, 0x3c800000, v60
	v_mul_f32_e32 v186, 0x3c800000, v186
	v_mul_f32_e32 v62, 0x3c800000, v62
	v_med3_f32 v188, v188, s73, v227
	v_med3_f32 v60, v60, s73, v227
	v_med3_f32 v186, v186, s73, v227
	v_med3_f32 v62, v62, s73, v227
	v_lshlrev_b32_e32 v203, 16, v61
	v_and_b32_e32 v61, 0xffff0000, v61
	v_and_b32_e32 v63, 0xffff0000, v63
	v_cvt_pk_fp8_f32 v64, v188, v60
	v_cvt_pk_fp8_f32 v65, v186, v62
	v_mul_f32_e32 v191, v192, v203
	v_mul_f32_e32 v61, v193, v61
	v_mul_f32_e32 v63, v189, v63
	v_mul_f32_e32 v189, 0x3c800000, v191
	v_mul_f32_e32 v61, 0x3c800000, v61
	v_mul_f32_e32 v187, 0x3c800000, v187
	v_mul_f32_e32 v63, 0x3c800000, v63
	v_med3_f32 v189, v189, s73, v227
	v_med3_f32 v61, v61, s73, v227
	v_med3_f32 v60, v187, s73, v227
	v_med3_f32 v62, v63, s73, v227
	v_cvt_pk_fp8_f32 v64, v189, v61 op_sel:[0,0,1]
	v_cvt_pk_fp8_f32 v65, v60, v62 op_sel:[0,0,1]
	v_lshlrev_b32_e32 v237, 16, v214
	v_and_b32_e32 v214, 0xffff0000, v214
	v_lshlrev_b32_e32 v60, 16, v215
	v_mul_f32_e32 v61, v182, v237
	v_mul_f32_e32 v62, v183, v214
	v_mov_b32_e32 v240, v64
	v_mov_b32_e32 v241, v65
	v_mul_f32_e32 v60, v184, v60
	v_lshlrev_b32_e32 v64, 16, v216
	v_and_b32_e32 v65, 0xffff0000, v216
	v_mul_f32_e32 v64, v178, v64
	v_mul_f32_e32 v65, v179, v65
	v_lshlrev_b32_e32 v178, 16, v217
	v_mul_f32_e32 v61, 0x3c800000, v61
	v_mul_f32_e32 v62, 0x3c800000, v62
	v_mul_f32_e32 v60, 0x3c800000, v60
	v_mul_f32_e32 v178, v180, v178
	v_mul_f32_e32 v64, 0x3c800000, v64
	v_mul_f32_e32 v65, 0x3c800000, v65
	v_med3_f32 v61, v61, s73, v227
	v_med3_f32 v62, v62, s73, v227
	v_med3_f32 v180, v60, s73, v227
	v_mov_b32_e32 v60, v199
	v_and_b32_e32 v63, 0xffff0000, v215
	v_cvt_pk_fp8_f32 v60, v61, v62
	v_med3_f32 v62, v64, s73, v227
	v_med3_f32 v64, v65, s73, v227
	v_mov_b32_e32 v61, v199
	v_mul_f32_e32 v63, v185, v63
	v_and_b32_e32 v179, 0xffff0000, v217
	v_cvt_pk_fp8_f32 v61, v62, v64
	v_mul_f32_e32 v179, v181, v179
	v_mul_f32_e32 v63, 0x3c800000, v63
	v_mul_f32_e32 v178, 0x3c800000, v178
	v_mul_f32_e32 v179, 0x3c800000, v179
	v_med3_f32 v63, v63, s73, v227
	v_cvt_pk_fp8_f32 v60, v180, v63 op_sel:[0,0,1]
	v_med3_f32 v62, v178, s73, v227
	v_med3_f32 v63, v179, s73, v227
	v_cvt_pk_fp8_f32 v61, v62, v63 op_sel:[0,0,1]
	v_lshl_add_u64 v[62:63], s[8:9], 0, v[212:213]
	v_lshl_add_u64 v[62:63], v[62:63], 0, v[210:211]
	v_add_co_u32_e32 v62, vcc, s74, v62
	v_lshlrev_b32_e32 v64, 16, v220
	s_nop 0
	v_addc_co_u32_e32 v63, vcc, 0, v63, vcc
	v_mov_b32_e32 v242, v60
	v_mov_b32_e32 v243, v61
	v_lshl_add_u64 v[248:249], v[62:63], 0, v[252:253]
	s_nop 1
	v_permlane16_swap_b32_e32 v240, v242
	v_permlane16_swap_b32_e32 v241, v243
	global_store_dwordx4 v[248:249], v[240:243], off
	v_lshlrev_b32_e32 v60, 16, v218
	v_and_b32_e32 v61, 0xffff0000, v218
	v_mul_f32_e32 v60, v174, v60
	v_mul_f32_e32 v61, v175, v61
	v_and_b32_e32 v65, 0xffff0000, v220
	v_mul_f32_e32 v64, v170, v64
	v_mul_f32_e32 v65, v171, v65
	v_lshlrev_b32_e32 v170, 16, v221
	v_mul_f32_e32 v60, 0x3c800000, v60
	v_mul_f32_e32 v61, 0x3c800000, v61
	v_mul_f32_e32 v170, v172, v170
	v_mul_f32_e32 v64, 0x3c800000, v64
	v_mul_f32_e32 v65, 0x3c800000, v65
	v_med3_f32 v172, v60, s73, v227
	v_med3_f32 v61, v61, s73, v227
	v_mov_b32_e32 v60, v199
	v_lshlrev_b32_e32 v62, 16, v219
	v_and_b32_e32 v63, 0xffff0000, v219
	v_cvt_pk_fp8_f32 v60, v172, v61
	v_med3_f32 v64, v64, s73, v227
	v_med3_f32 v65, v65, s73, v227
	v_mov_b32_e32 v61, v199
	v_mul_f32_e32 v62, v176, v62
	v_mul_f32_e32 v63, v177, v63
	v_and_b32_e32 v171, 0xffff0000, v221
	v_cvt_pk_fp8_f32 v61, v64, v65
	v_mul_f32_e32 v171, v173, v171
	v_mul_f32_e32 v62, 0x3c800000, v62
	v_mul_f32_e32 v63, 0x3c800000, v63
	v_mul_f32_e32 v170, 0x3c800000, v170
	v_mul_f32_e32 v171, 0x3c800000, v171
	v_med3_f32 v62, v62, s73, v227
	v_med3_f32 v63, v63, s73, v227
	v_cvt_pk_fp8_f32 v60, v62, v63 op_sel:[0,0,1]
	v_med3_f32 v62, v170, s73, v227
	v_med3_f32 v63, v171, s73, v227
	v_cvt_pk_fp8_f32 v61, v62, v63 op_sel:[0,0,1]
	v_lshl_add_u64 v[62:63], s[26:27], 0, v[58:59]
	v_lshl_add_u64 v[62:63], v[62:63], 0, v[210:211]
	v_lshlrev_b32_e32 v64, 16, v230
	v_mov_b32_e32 v244, v60
	v_mov_b32_e32 v245, v61
	v_lshlrev_b32_e32 v60, 16, v228
	v_and_b32_e32 v61, 0xffff0000, v228
	v_mul_f32_e32 v60, v166, v60
	v_mul_f32_e32 v61, v167, v61
	v_and_b32_e32 v65, 0xffff0000, v230
	v_mul_f32_e32 v64, v162, v64
	v_mul_f32_e32 v65, v163, v65
	v_lshlrev_b32_e32 v162, 16, v231
	v_mul_f32_e32 v60, 0x3c800000, v60
	v_mul_f32_e32 v61, 0x3c800000, v61
	v_mul_f32_e32 v162, v164, v162
	v_mul_f32_e32 v64, 0x3c800000, v64
	v_mul_f32_e32 v65, 0x3c800000, v65
	v_med3_f32 v164, v60, s73, v227
	v_med3_f32 v61, v61, s73, v227
	v_mov_b32_e32 v60, v199
	v_lshlrev_b32_e32 v62, 16, v229
	v_and_b32_e32 v63, 0xffff0000, v229
	v_cvt_pk_fp8_f32 v60, v164, v61
	v_med3_f32 v64, v64, s73, v227
	v_med3_f32 v65, v65, s73, v227
	v_mov_b32_e32 v61, v199
	v_mul_f32_e32 v62, v168, v62
	v_mul_f32_e32 v63, v169, v63
	v_and_b32_e32 v163, 0xffff0000, v231
	v_cvt_pk_fp8_f32 v61, v64, v65
	v_mul_f32_e32 v163, v165, v163
	v_mul_f32_e32 v62, 0x3c800000, v62
	v_mul_f32_e32 v63, 0x3c800000, v63
	v_mul_f32_e32 v162, 0x3c800000, v162
	v_mul_f32_e32 v163, 0x3c800000, v163
	v_med3_f32 v62, v62, s73, v227
	v_med3_f32 v63, v63, s73, v227
	v_cvt_pk_fp8_f32 v60, v62, v63 op_sel:[0,0,1]
	v_med3_f32 v62, v162, s73, v227
	v_med3_f32 v63, v163, s73, v227
	v_cvt_pk_fp8_f32 v61, v62, v63 op_sel:[0,0,1]
	v_lshl_add_u64 v[58:59], s[8:9], 0, v[58:59]
	v_lshl_add_u64 v[58:59], v[58:59], 0, v[210:211]
	v_add_co_u32_e32 v58, vcc, s74, v58
	v_lshlrev_b32_e32 v62, 16, v234
	s_nop 0
	v_addc_co_u32_e32 v59, vcc, 0, v59, vcc
	v_mov_b32_e32 v246, v60
	v_mov_b32_e32 v247, v61
	v_lshl_add_u64 v[250:251], v[58:59], 0, v[252:253]
	s_nop 1
	v_permlane16_swap_b32_e32 v244, v246
	v_permlane16_swap_b32_e32 v245, v247
	global_store_dwordx4 v[250:251], v[244:247], off
	v_lshlrev_b32_e32 v58, 16, v232
	v_and_b32_e32 v59, 0xffff0000, v232
	v_mul_f32_e32 v58, v158, v58
	v_mul_f32_e32 v59, v159, v59
	v_and_b32_e32 v63, 0xffff0000, v234
	v_mul_f32_e32 v62, v154, v62
	v_mul_f32_e32 v63, v155, v63
	v_mul_f32_e32 v58, 0x3c800000, v58
	v_mul_f32_e32 v59, 0x3c800000, v59
	v_mul_f32_e32 v62, 0x3c800000, v62
	v_mul_f32_e32 v63, 0x3c800000, v63
	v_med3_f32 v154, v58, s73, v227
	v_med3_f32 v59, v59, s73, v227
	v_mov_b32_e32 v58, v199
	v_lshlrev_b32_e32 v60, 16, v233
	v_and_b32_e32 v61, 0xffff0000, v233
	v_cvt_pk_fp8_f32 v58, v154, v59
	v_med3_f32 v62, v62, s73, v227
	v_med3_f32 v63, v63, s73, v227
	v_mov_b32_e32 v59, v199
	v_mul_f32_e32 v60, v160, v60
	v_mul_f32_e32 v61, v161, v61
	v_lshlrev_b32_e32 v64, 16, v235
	v_and_b32_e32 v65, 0xffff0000, v235
	v_cvt_pk_fp8_f32 v59, v62, v63
	v_mul_f32_e32 v64, v156, v64
	v_mul_f32_e32 v65, v157, v65
	v_mul_f32_e32 v60, 0x3c800000, v60
	v_mul_f32_e32 v61, 0x3c800000, v61
	v_mul_f32_e32 v64, 0x3c800000, v64
	v_mul_f32_e32 v65, 0x3c800000, v65
	v_med3_f32 v60, v60, s73, v227
	v_med3_f32 v61, v61, s73, v227
	v_cvt_pk_fp8_f32 v58, v60, v61 op_sel:[0,0,1]
	v_med3_f32 v60, v64, s73, v227
	v_med3_f32 v61, v65, s73, v227
	v_cvt_pk_fp8_f32 v59, v60, v61 op_sel:[0,0,1]
	v_lshl_add_u64 v[60:61], s[26:27], 0, v[56:57]
	v_lshl_add_u64 v[60:61], v[60:61], 0, v[210:211]
	v_mov_b32_e32 v240, v58
	v_mov_b32_e32 v241, v59
	v_lshlrev_b32_e32 v58, 16, v42
	v_and_b32_e32 v42, 0xffff0000, v42
	v_mul_f32_e32 v58, v150, v58
	v_mul_f32_e32 v42, v151, v42
	v_lshlrev_b32_e32 v59, 16, v43
	v_and_b32_e32 v43, 0xffff0000, v43
	v_lshlrev_b32_e32 v60, 16, v44
	v_and_b32_e32 v44, 0xffff0000, v44
	v_mul_f32_e32 v43, v153, v43
	v_mul_f32_e32 v60, v146, v60
	v_mul_f32_e32 v44, v147, v44
	v_mul_f32_e32 v58, 0x3c800000, v58
	v_mul_f32_e32 v42, 0x3c800000, v42
	v_mul_f32_e32 v43, 0x3c800000, v43
	v_mul_f32_e32 v60, 0x3c800000, v60
	v_mul_f32_e32 v44, 0x3c800000, v44
	v_med3_f32 v58, v58, s73, v227
	v_med3_f32 v62, v42, s73, v227
	v_mov_b32_e32 v42, v199
	v_med3_f32 v63, v43, s73, v227
	v_cvt_pk_fp8_f32 v42, v58, v62
	v_med3_f32 v58, v60, s73, v227
	v_med3_f32 v44, v44, s73, v227
	v_mov_b32_e32 v43, v199
	v_lshlrev_b32_e32 v61, 16, v45
	v_and_b32_e32 v45, 0xffff0000, v45
	v_cvt_pk_fp8_f32 v43, v58, v44
	v_mul_f32_e32 v59, v152, v59
	v_mul_f32_e32 v61, v148, v61
	v_mul_f32_e32 v45, v149, v45
	v_mul_f32_e32 v59, 0x3c800000, v59
	v_mul_f32_e32 v61, 0x3c800000, v61
	v_mul_f32_e32 v45, 0x3c800000, v45
	v_med3_f32 v59, v59, s73, v227
	v_med3_f32 v44, v61, s73, v227
	v_med3_f32 v45, v45, s73, v227
	v_cvt_pk_fp8_f32 v42, v59, v63 op_sel:[0,0,1]
	v_cvt_pk_fp8_f32 v43, v44, v45 op_sel:[0,0,1]
	v_lshl_add_u64 v[44:45], s[8:9], 0, v[56:57]
	v_lshl_add_u64 v[44:45], v[44:45], 0, v[210:211]
	v_add_co_u32_e32 v44, vcc, s74, v44
	s_nop 1
	v_addc_co_u32_e32 v45, vcc, 0, v45, vcc
	v_mov_b32_e32 v242, v42
	v_mov_b32_e32 v243, v43
	v_lshl_add_u64 v[248:249], v[44:45], 0, v[252:253]
	s_nop 1
	v_permlane16_swap_b32_e32 v240, v242
	v_permlane16_swap_b32_e32 v241, v243
	global_store_dwordx4 v[248:249], v[240:243], off
	v_lshlrev_b32_e32 v42, 16, v38
	v_and_b32_e32 v38, 0xffff0000, v38
	v_mul_f32_e32 v42, v142, v42
	v_mul_f32_e32 v38, v143, v38
	v_lshlrev_b32_e32 v43, 16, v39
	v_and_b32_e32 v39, 0xffff0000, v39
	v_lshlrev_b32_e32 v44, 16, v40
	v_and_b32_e32 v40, 0xffff0000, v40
	v_mul_f32_e32 v39, v145, v39
	v_mul_f32_e32 v44, v138, v44
	v_mul_f32_e32 v40, v139, v40
	v_mul_f32_e32 v42, 0x3c800000, v42
	v_mul_f32_e32 v38, 0x3c800000, v38
	v_mul_f32_e32 v39, 0x3c800000, v39
	v_mul_f32_e32 v44, 0x3c800000, v44
	v_mul_f32_e32 v40, 0x3c800000, v40
	v_med3_f32 v42, v42, s73, v227
	v_med3_f32 v56, v38, s73, v227
	v_mov_b32_e32 v38, v199
	v_med3_f32 v57, v39, s73, v227
	v_cvt_pk_fp8_f32 v38, v42, v56
	v_med3_f32 v42, v44, s73, v227
	v_med3_f32 v40, v40, s73, v227
	v_mov_b32_e32 v39, v199
	v_lshlrev_b32_e32 v45, 16, v41
	v_and_b32_e32 v41, 0xffff0000, v41
	v_cvt_pk_fp8_f32 v39, v42, v40
	v_mul_f32_e32 v43, v144, v43
	v_mul_f32_e32 v45, v140, v45
	v_mul_f32_e32 v41, v141, v41
	v_mul_f32_e32 v43, 0x3c800000, v43
	v_mul_f32_e32 v45, 0x3c800000, v45
	v_mul_f32_e32 v41, 0x3c800000, v41
	v_med3_f32 v43, v43, s73, v227
	v_med3_f32 v40, v45, s73, v227
	v_med3_f32 v41, v41, s73, v227
	v_cvt_pk_fp8_f32 v38, v43, v57 op_sel:[0,0,1]
	v_cvt_pk_fp8_f32 v39, v40, v41 op_sel:[0,0,1]
	v_lshlrev_b64 v[40:41], 11, v[54:55]
	v_lshl_add_u64 v[42:43], s[26:27], 0, v[40:41]
	v_lshl_add_u64 v[42:43], v[42:43], 0, v[210:211]
	v_mov_b32_e32 v244, v38
	v_mov_b32_e32 v245, v39
	v_lshlrev_b32_e32 v38, 16, v34
	v_and_b32_e32 v34, 0xffff0000, v34
	v_mul_f32_e32 v38, v134, v38
	v_mul_f32_e32 v34, v135, v34
	v_lshlrev_b32_e32 v39, 16, v35
	v_and_b32_e32 v35, 0xffff0000, v35
	v_lshlrev_b32_e32 v42, 16, v36
	v_and_b32_e32 v36, 0xffff0000, v36
	v_mul_f32_e32 v35, v137, v35
	v_mul_f32_e32 v42, v130, v42
	v_mul_f32_e32 v36, v131, v36
	v_mul_f32_e32 v38, 0x3c800000, v38
	v_mul_f32_e32 v34, 0x3c800000, v34
	v_mul_f32_e32 v35, 0x3c800000, v35
	v_mul_f32_e32 v42, 0x3c800000, v42
	v_mul_f32_e32 v36, 0x3c800000, v36
	v_med3_f32 v38, v38, s73, v227
	v_med3_f32 v44, v34, s73, v227
	v_mov_b32_e32 v34, v199
	v_med3_f32 v45, v35, s73, v227
	v_cvt_pk_fp8_f32 v34, v38, v44
	v_med3_f32 v38, v42, s73, v227
	v_med3_f32 v36, v36, s73, v227
	v_mov_b32_e32 v35, v199
	v_lshlrev_b32_e32 v43, 16, v37
	v_and_b32_e32 v37, 0xffff0000, v37
	v_cvt_pk_fp8_f32 v35, v38, v36
	v_mul_f32_e32 v39, v136, v39
	v_mul_f32_e32 v43, v132, v43
	v_mul_f32_e32 v37, v133, v37
	v_mul_f32_e32 v39, 0x3c800000, v39
	v_mul_f32_e32 v43, 0x3c800000, v43
	v_mul_f32_e32 v37, 0x3c800000, v37
	v_med3_f32 v39, v39, s73, v227
	v_med3_f32 v36, v43, s73, v227
	v_med3_f32 v37, v37, s73, v227
	v_cvt_pk_fp8_f32 v34, v39, v45 op_sel:[0,0,1]
	v_cvt_pk_fp8_f32 v35, v36, v37 op_sel:[0,0,1]
	v_lshl_add_u64 v[36:37], s[8:9], 0, v[40:41]
	v_lshl_add_u64 v[36:37], v[36:37], 0, v[210:211]
	v_add_co_u32_e32 v36, vcc, s74, v36
	s_nop 1
	v_addc_co_u32_e32 v37, vcc, 0, v37, vcc
	v_mov_b32_e32 v246, v34
	v_mov_b32_e32 v247, v35
	v_lshl_add_u64 v[250:251], v[36:37], 0, v[252:253]
	s_nop 1
	v_permlane16_swap_b32_e32 v244, v246
	v_permlane16_swap_b32_e32 v245, v247
	global_store_dwordx4 v[250:251], v[244:247], off
	v_lshlrev_b32_e32 v34, 16, v30
	v_and_b32_e32 v30, 0xffff0000, v30
	v_mul_f32_e32 v34, v126, v34
	v_mul_f32_e32 v30, v127, v30
	v_lshlrev_b32_e32 v35, 16, v31
	v_and_b32_e32 v31, 0xffff0000, v31
	v_lshlrev_b32_e32 v36, 16, v32
	v_and_b32_e32 v32, 0xffff0000, v32
	v_mul_f32_e32 v31, v129, v31
	v_mul_f32_e32 v36, v122, v36
	v_mul_f32_e32 v32, v123, v32
	v_mul_f32_e32 v34, 0x3c800000, v34
	v_mul_f32_e32 v30, 0x3c800000, v30
	v_mul_f32_e32 v31, 0x3c800000, v31
	v_mul_f32_e32 v36, 0x3c800000, v36
	v_mul_f32_e32 v32, 0x3c800000, v32
	v_med3_f32 v34, v34, s73, v227
	v_med3_f32 v38, v30, s73, v227
	v_mov_b32_e32 v30, v199
	v_med3_f32 v39, v31, s73, v227
	v_cvt_pk_fp8_f32 v30, v34, v38
	v_med3_f32 v34, v36, s73, v227
	v_med3_f32 v32, v32, s73, v227
	v_mov_b32_e32 v31, v199
	v_lshlrev_b32_e32 v37, 16, v33
	v_and_b32_e32 v33, 0xffff0000, v33
	v_cvt_pk_fp8_f32 v31, v34, v32
	v_mul_f32_e32 v35, v128, v35
	v_mul_f32_e32 v37, v124, v37
	v_mul_f32_e32 v33, v125, v33
	v_mul_f32_e32 v35, 0x3c800000, v35
	v_mul_f32_e32 v37, 0x3c800000, v37
	v_mul_f32_e32 v33, 0x3c800000, v33
	v_med3_f32 v35, v35, s73, v227
	v_med3_f32 v32, v37, s73, v227
	v_med3_f32 v33, v33, s73, v227
	v_cvt_pk_fp8_f32 v30, v35, v39 op_sel:[0,0,1]
	v_cvt_pk_fp8_f32 v31, v32, v33 op_sel:[0,0,1]
	v_lshlrev_b64 v[32:33], 11, v[52:53]
	v_lshl_add_u64 v[34:35], s[26:27], 0, v[32:33]
	v_lshl_add_u64 v[34:35], v[34:35], 0, v[210:211]
	v_mov_b32_e32 v240, v30
	v_mov_b32_e32 v241, v31
	v_lshlrev_b32_e32 v30, 16, v26
	v_and_b32_e32 v26, 0xffff0000, v26
	v_mul_f32_e32 v30, v118, v30
	v_mul_f32_e32 v26, v119, v26
	v_lshlrev_b32_e32 v31, 16, v27
	v_and_b32_e32 v27, 0xffff0000, v27
	v_lshlrev_b32_e32 v34, 16, v28
	v_and_b32_e32 v28, 0xffff0000, v28
	v_mul_f32_e32 v27, v121, v27
	v_mul_f32_e32 v34, v114, v34
	v_mul_f32_e32 v28, v115, v28
	v_mul_f32_e32 v30, 0x3c800000, v30
	v_mul_f32_e32 v26, 0x3c800000, v26
	v_mul_f32_e32 v27, 0x3c800000, v27
	v_mul_f32_e32 v34, 0x3c800000, v34
	v_mul_f32_e32 v28, 0x3c800000, v28
	v_med3_f32 v30, v30, s73, v227
	v_med3_f32 v36, v26, s73, v227
	v_mov_b32_e32 v26, v199
	v_med3_f32 v37, v27, s73, v227
	v_cvt_pk_fp8_f32 v26, v30, v36
	v_med3_f32 v30, v34, s73, v227
	v_med3_f32 v28, v28, s73, v227
	v_mov_b32_e32 v27, v199
	v_lshlrev_b32_e32 v35, 16, v29
	v_and_b32_e32 v29, 0xffff0000, v29
	v_cvt_pk_fp8_f32 v27, v30, v28
	v_mul_f32_e32 v31, v120, v31
	v_mul_f32_e32 v35, v116, v35
	v_mul_f32_e32 v29, v117, v29
	v_mul_f32_e32 v31, 0x3c800000, v31
	v_mul_f32_e32 v35, 0x3c800000, v35
	v_mul_f32_e32 v29, 0x3c800000, v29
	v_med3_f32 v31, v31, s73, v227
	v_med3_f32 v28, v35, s73, v227
	v_med3_f32 v29, v29, s73, v227
	v_cvt_pk_fp8_f32 v26, v31, v37 op_sel:[0,0,1]
	v_cvt_pk_fp8_f32 v27, v28, v29 op_sel:[0,0,1]
	v_lshl_add_u64 v[28:29], s[8:9], 0, v[32:33]
	v_lshl_add_u64 v[28:29], v[28:29], 0, v[210:211]
	v_add_co_u32_e32 v28, vcc, s74, v28
	s_nop 1
	v_addc_co_u32_e32 v29, vcc, 0, v29, vcc
	v_mov_b32_e32 v242, v26
	v_mov_b32_e32 v243, v27
	v_lshl_add_u64 v[248:249], v[28:29], 0, v[252:253]
	s_nop 1
	v_permlane16_swap_b32_e32 v240, v242
	v_permlane16_swap_b32_e32 v241, v243
	global_store_dwordx4 v[248:249], v[240:243], off
	v_lshlrev_b32_e32 v26, 16, v22
	v_and_b32_e32 v22, 0xffff0000, v22
	v_mul_f32_e32 v26, v110, v26
	v_mul_f32_e32 v22, v111, v22
	v_lshlrev_b32_e32 v27, 16, v23
	v_and_b32_e32 v23, 0xffff0000, v23
	v_lshlrev_b32_e32 v28, 16, v24
	v_and_b32_e32 v24, 0xffff0000, v24
	v_mul_f32_e32 v23, v113, v23
	v_mul_f32_e32 v28, v106, v28
	v_mul_f32_e32 v24, v107, v24
	v_mul_f32_e32 v26, 0x3c800000, v26
	v_mul_f32_e32 v22, 0x3c800000, v22
	v_mul_f32_e32 v23, 0x3c800000, v23
	v_mul_f32_e32 v28, 0x3c800000, v28
	v_mul_f32_e32 v24, 0x3c800000, v24
	v_med3_f32 v26, v26, s73, v227
	v_med3_f32 v30, v22, s73, v227
	v_mov_b32_e32 v22, v199
	v_med3_f32 v31, v23, s73, v227
	v_cvt_pk_fp8_f32 v22, v26, v30
	v_med3_f32 v26, v28, s73, v227
	v_med3_f32 v24, v24, s73, v227
	v_mov_b32_e32 v23, v199
	v_lshlrev_b32_e32 v29, 16, v25
	v_and_b32_e32 v25, 0xffff0000, v25
	v_cvt_pk_fp8_f32 v23, v26, v24
	v_mul_f32_e32 v27, v112, v27
	v_mul_f32_e32 v29, v108, v29
	v_mul_f32_e32 v25, v109, v25
	v_mul_f32_e32 v27, 0x3c800000, v27
	v_mul_f32_e32 v29, 0x3c800000, v29
	v_mul_f32_e32 v25, 0x3c800000, v25
	v_med3_f32 v27, v27, s73, v227
	v_med3_f32 v24, v29, s73, v227
	v_med3_f32 v25, v25, s73, v227
	v_cvt_pk_fp8_f32 v22, v27, v31 op_sel:[0,0,1]
	v_cvt_pk_fp8_f32 v23, v24, v25 op_sel:[0,0,1]
	v_lshlrev_b64 v[24:25], 11, v[50:51]
	v_lshl_add_u64 v[26:27], s[26:27], 0, v[24:25]
	v_lshl_add_u64 v[26:27], v[26:27], 0, v[210:211]
	v_mov_b32_e32 v244, v22
	v_mov_b32_e32 v245, v23
	v_lshlrev_b32_e32 v22, 16, v18
	v_and_b32_e32 v18, 0xffff0000, v18
	v_mul_f32_e32 v22, v102, v22
	v_mul_f32_e32 v18, v103, v18
	v_lshlrev_b32_e32 v23, 16, v19
	v_and_b32_e32 v19, 0xffff0000, v19
	v_lshlrev_b32_e32 v26, 16, v20
	v_and_b32_e32 v20, 0xffff0000, v20
	v_mul_f32_e32 v19, v105, v19
	v_mul_f32_e32 v26, v98, v26
	v_mul_f32_e32 v20, v99, v20
	v_mul_f32_e32 v22, 0x3c800000, v22
	v_mul_f32_e32 v18, 0x3c800000, v18
	v_mul_f32_e32 v19, 0x3c800000, v19
	v_mul_f32_e32 v26, 0x3c800000, v26
	v_mul_f32_e32 v20, 0x3c800000, v20
	v_med3_f32 v22, v22, s73, v227
	v_med3_f32 v28, v18, s73, v227
	v_mov_b32_e32 v18, v199
	v_med3_f32 v29, v19, s73, v227
	v_cvt_pk_fp8_f32 v18, v22, v28
	v_med3_f32 v22, v26, s73, v227
	v_med3_f32 v20, v20, s73, v227
	v_mov_b32_e32 v19, v199
	v_lshlrev_b32_e32 v27, 16, v21
	v_and_b32_e32 v21, 0xffff0000, v21
	v_cvt_pk_fp8_f32 v19, v22, v20
	v_mul_f32_e32 v23, v104, v23
	v_mul_f32_e32 v27, v100, v27
	v_mul_f32_e32 v21, v101, v21
	v_mul_f32_e32 v23, 0x3c800000, v23
	v_mul_f32_e32 v27, 0x3c800000, v27
	v_mul_f32_e32 v21, 0x3c800000, v21
	v_med3_f32 v23, v23, s73, v227
	v_med3_f32 v20, v27, s73, v227
	v_med3_f32 v21, v21, s73, v227
	v_cvt_pk_fp8_f32 v18, v23, v29 op_sel:[0,0,1]
	v_cvt_pk_fp8_f32 v19, v20, v21 op_sel:[0,0,1]
	v_lshl_add_u64 v[20:21], s[8:9], 0, v[24:25]
	v_lshl_add_u64 v[20:21], v[20:21], 0, v[210:211]
	v_add_co_u32_e32 v20, vcc, s74, v20
	s_nop 1
	v_addc_co_u32_e32 v21, vcc, 0, v21, vcc
	v_mov_b32_e32 v246, v18
	v_mov_b32_e32 v247, v19
	v_lshl_add_u64 v[250:251], v[20:21], 0, v[252:253]
	s_nop 1
	v_permlane16_swap_b32_e32 v244, v246
	v_permlane16_swap_b32_e32 v245, v247
	global_store_dwordx4 v[250:251], v[244:247], off
	v_lshlrev_b32_e32 v18, 16, v14
	v_and_b32_e32 v14, 0xffff0000, v14
	v_mul_f32_e32 v18, v94, v18
	v_mul_f32_e32 v14, v95, v14
	v_lshlrev_b32_e32 v19, 16, v15
	v_and_b32_e32 v15, 0xffff0000, v15
	v_lshlrev_b32_e32 v20, 16, v16
	v_and_b32_e32 v16, 0xffff0000, v16
	v_mul_f32_e32 v15, v97, v15
	v_mul_f32_e32 v20, v90, v20
	v_mul_f32_e32 v16, v91, v16
	v_mul_f32_e32 v18, 0x3c800000, v18
	v_mul_f32_e32 v14, 0x3c800000, v14
	v_mul_f32_e32 v15, 0x3c800000, v15
	v_mul_f32_e32 v20, 0x3c800000, v20
	v_mul_f32_e32 v16, 0x3c800000, v16
	v_med3_f32 v18, v18, s73, v227
	v_med3_f32 v22, v14, s73, v227
	v_mov_b32_e32 v14, v199
	v_med3_f32 v23, v15, s73, v227
	v_cvt_pk_fp8_f32 v14, v18, v22
	v_med3_f32 v18, v20, s73, v227
	v_med3_f32 v16, v16, s73, v227
	v_mov_b32_e32 v15, v199
	v_lshlrev_b32_e32 v21, 16, v17
	v_and_b32_e32 v17, 0xffff0000, v17
	v_cvt_pk_fp8_f32 v15, v18, v16
	v_mul_f32_e32 v19, v96, v19
	v_mul_f32_e32 v21, v92, v21
	v_mul_f32_e32 v17, v93, v17
	v_mul_f32_e32 v19, 0x3c800000, v19
	v_mul_f32_e32 v21, 0x3c800000, v21
	v_mul_f32_e32 v17, 0x3c800000, v17
	v_med3_f32 v19, v19, s73, v227
	v_med3_f32 v16, v21, s73, v227
	v_med3_f32 v17, v17, s73, v227
	v_cvt_pk_fp8_f32 v14, v19, v23 op_sel:[0,0,1]
	v_cvt_pk_fp8_f32 v15, v16, v17 op_sel:[0,0,1]
	v_lshlrev_b64 v[16:17], 11, v[48:49]
	v_lshl_add_u64 v[18:19], s[26:27], 0, v[16:17]
	v_lshl_add_u64 v[18:19], v[18:19], 0, v[210:211]
	v_mov_b32_e32 v240, v14
	v_mov_b32_e32 v241, v15
	v_lshlrev_b32_e32 v14, 16, v10
	v_and_b32_e32 v10, 0xffff0000, v10
	v_mul_f32_e32 v14, v86, v14
	v_mul_f32_e32 v10, v87, v10
	v_lshlrev_b32_e32 v15, 16, v11
	v_and_b32_e32 v11, 0xffff0000, v11
	v_lshlrev_b32_e32 v18, 16, v12
	v_and_b32_e32 v12, 0xffff0000, v12
	v_mul_f32_e32 v11, v89, v11
	v_mul_f32_e32 v18, v82, v18
	v_mul_f32_e32 v12, v83, v12
	v_mul_f32_e32 v14, 0x3c800000, v14
	v_mul_f32_e32 v10, 0x3c800000, v10
	v_mul_f32_e32 v11, 0x3c800000, v11
	v_mul_f32_e32 v18, 0x3c800000, v18
	v_mul_f32_e32 v12, 0x3c800000, v12
	v_med3_f32 v14, v14, s73, v227
	v_med3_f32 v20, v10, s73, v227
	v_mov_b32_e32 v10, v199
	v_med3_f32 v21, v11, s73, v227
	v_cvt_pk_fp8_f32 v10, v14, v20
	v_med3_f32 v14, v18, s73, v227
	v_med3_f32 v12, v12, s73, v227
	v_mov_b32_e32 v11, v199
	v_lshlrev_b32_e32 v19, 16, v13
	v_and_b32_e32 v13, 0xffff0000, v13
	v_cvt_pk_fp8_f32 v11, v14, v12
	v_mul_f32_e32 v15, v88, v15
	v_mul_f32_e32 v19, v84, v19
	v_mul_f32_e32 v13, v85, v13
	v_mul_f32_e32 v15, 0x3c800000, v15
	v_mul_f32_e32 v19, 0x3c800000, v19
	v_mul_f32_e32 v13, 0x3c800000, v13
	v_med3_f32 v15, v15, s73, v227
	v_med3_f32 v12, v19, s73, v227
	v_med3_f32 v13, v13, s73, v227
	v_cvt_pk_fp8_f32 v10, v15, v21 op_sel:[0,0,1]
	v_cvt_pk_fp8_f32 v11, v12, v13 op_sel:[0,0,1]
	v_lshl_add_u64 v[12:13], s[8:9], 0, v[16:17]
	v_lshl_add_u64 v[12:13], v[12:13], 0, v[210:211]
	v_add_co_u32_e32 v12, vcc, s74, v12
	s_nop 1
	v_addc_co_u32_e32 v13, vcc, 0, v13, vcc
	v_mov_b32_e32 v242, v10
	v_mov_b32_e32 v243, v11
	v_lshl_add_u64 v[248:249], v[12:13], 0, v[252:253]
	s_nop 1
	v_permlane16_swap_b32_e32 v240, v242
	v_permlane16_swap_b32_e32 v241, v243
	global_store_dwordx4 v[248:249], v[240:243], off
	v_lshlrev_b32_e32 v10, 16, v6
	v_and_b32_e32 v6, 0xffff0000, v6
	v_mul_f32_e32 v10, v78, v10
	v_mul_f32_e32 v6, v79, v6
	v_lshlrev_b32_e32 v11, 16, v7
	v_and_b32_e32 v7, 0xffff0000, v7
	v_lshlrev_b32_e32 v12, 16, v8
	v_and_b32_e32 v8, 0xffff0000, v8
	v_mul_f32_e32 v7, v81, v7
	v_mul_f32_e32 v12, v74, v12
	v_mul_f32_e32 v8, v75, v8
	v_mul_f32_e32 v10, 0x3c800000, v10
	v_mul_f32_e32 v6, 0x3c800000, v6
	v_mul_f32_e32 v7, 0x3c800000, v7
	v_mul_f32_e32 v12, 0x3c800000, v12
	v_mul_f32_e32 v8, 0x3c800000, v8
	v_med3_f32 v10, v10, s73, v227
	v_med3_f32 v14, v6, s73, v227
	v_mov_b32_e32 v6, v199
	v_med3_f32 v15, v7, s73, v227
	v_cvt_pk_fp8_f32 v6, v10, v14
	v_med3_f32 v10, v12, s73, v227
	v_med3_f32 v8, v8, s73, v227
	v_mov_b32_e32 v7, v199
	v_lshlrev_b32_e32 v13, 16, v9
	v_and_b32_e32 v9, 0xffff0000, v9
	v_cvt_pk_fp8_f32 v7, v10, v8
	v_mul_f32_e32 v11, v80, v11
	v_mul_f32_e32 v13, v76, v13
	v_mul_f32_e32 v9, v77, v9
	v_mul_f32_e32 v11, 0x3c800000, v11
	v_mul_f32_e32 v13, 0x3c800000, v13
	v_mul_f32_e32 v9, 0x3c800000, v9
	v_med3_f32 v11, v11, s73, v227
	v_med3_f32 v8, v13, s73, v227
	v_med3_f32 v9, v9, s73, v227
	v_cvt_pk_fp8_f32 v6, v11, v15 op_sel:[0,0,1]
	v_cvt_pk_fp8_f32 v7, v8, v9 op_sel:[0,0,1]
	v_lshlrev_b64 v[8:9], 11, v[46:47]
	v_lshl_add_u64 v[10:11], s[26:27], 0, v[8:9]
	v_lshl_add_u64 v[10:11], v[10:11], 0, v[210:211]
	v_mov_b32_e32 v244, v6
	v_mov_b32_e32 v245, v7
	v_lshlrev_b32_e32 v6, 16, v2
	v_and_b32_e32 v2, 0xffff0000, v2
	v_mul_f32_e32 v6, v70, v6
	v_mul_f32_e32 v2, v71, v2
	v_lshlrev_b32_e32 v7, 16, v3
	v_and_b32_e32 v3, 0xffff0000, v3
	v_lshlrev_b32_e32 v10, 16, v4
	v_and_b32_e32 v4, 0xffff0000, v4
	v_mul_f32_e32 v3, v73, v3
	v_mul_f32_e32 v10, v66, v10
	v_mul_f32_e32 v4, v67, v4
	v_mul_f32_e32 v6, 0x3c800000, v6
	v_mul_f32_e32 v2, 0x3c800000, v2
	v_mul_f32_e32 v3, 0x3c800000, v3
	v_mul_f32_e32 v10, 0x3c800000, v10
	v_mul_f32_e32 v4, 0x3c800000, v4
	v_med3_f32 v6, v6, s73, v227
	v_med3_f32 v12, v2, s73, v227
	v_mov_b32_e32 v2, v199
	v_med3_f32 v13, v3, s73, v227
	v_cvt_pk_fp8_f32 v2, v6, v12
	v_med3_f32 v6, v10, s73, v227
	v_med3_f32 v4, v4, s73, v227
	v_mov_b32_e32 v3, v199
	v_lshlrev_b32_e32 v11, 16, v5
	v_and_b32_e32 v5, 0xffff0000, v5
	v_cvt_pk_fp8_f32 v3, v6, v4
	v_mul_f32_e32 v11, v68, v11
	v_mul_f32_e32 v5, v69, v5
	v_mul_f32_e32 v7, v72, v7
	v_mul_f32_e32 v11, 0x3c800000, v11
	v_mul_f32_e32 v5, 0x3c800000, v5
	v_mul_f32_e32 v7, 0x3c800000, v7
	v_med3_f32 v4, v11, s73, v227
	v_med3_f32 v5, v5, s73, v227
	v_med3_f32 v7, v7, s73, v227
	v_cvt_pk_fp8_f32 v3, v4, v5 op_sel:[0,0,1]
	v_lshl_add_u64 v[4:5], s[8:9], 0, v[8:9]
	v_cvt_pk_fp8_f32 v2, v7, v13 op_sel:[0,0,1]
	v_lshl_add_u64 v[4:5], v[4:5], 0, v[210:211]
	v_add_co_u32_e32 v4, vcc, 0x24c00000, v4
	s_nop 1
	v_addc_co_u32_e32 v5, vcc, 0, v5, vcc
	s_and_b64 vcc, exec, s[0:1]
	s_mov_b64 s[0:1], -1
	v_mov_b32_e32 v246, v2
	v_mov_b32_e32 v247, v3
	v_lshl_add_u64 v[250:251], v[4:5], 0, v[252:253]
	s_nop 1
	v_permlane16_swap_b32_e32 v244, v246
	v_permlane16_swap_b32_e32 v245, v247
	global_store_dwordx4 v[250:251], v[244:247], off
	s_cbranch_vccnz .LBB0_1098
	s_andn2_b64 vcc, exec, s[16:17]
	s_cbranch_vccnz .LBB0_1097
	s_barrier
	s_branch .LBB0_1097

.LBB0_1478:
	v_mbcnt_lo_u32_b32 v52, -1, 0
	v_mbcnt_hi_u32_b32 v52, -1, v52
	v_bfe_u32 v52, v52, 4, 1
	v_mul_u32_u24_e32 v52, 0x78, v52
	v_mov_b32_e32 v53, 0
	v_lshl_or_b32 v2, s30, 8, v234
	v_ashrrev_i32_e32 v3, 31, v2
	v_lshl_add_u64 v[2:3], s[26:27], 0, v[2:3]
	v_cmp_lt_i32_e32 vcc, v225, v224
	s_and_saveexec_b64 s[4:5], vcc
	s_cbranch_execnz .LBB0_1487
	s_or_b64 exec, exec, s[4:5]
	v_cmp_lt_i32_e32 vcc, v227, v224
	s_and_saveexec_b64 s[4:5], vcc
	s_cbranch_execnz .LBB0_1488

.LBB0_1487:
	v_mul_f32_e32 v4, 0x3e000000, v189
	v_med3_f32 v6, v4, s58, v237
	v_mul_f32_e32 v4, 0x3e000000, v190
	v_med3_f32 v5, v4, s58, v237
	v_mul_f32_e32 v4, 0x3e000000, v191
	v_med3_f32 v7, v4, s58, v237
	v_mul_f32_e32 v4, 0x3e000000, v192
	v_med3_f32 v8, v4, s58, v237
	v_mul_f32_e32 v4, 0x3e000000, v193
	v_med3_f32 v9, v4, s58, v237
	v_mul_f32_e32 v4, 0x3e000000, v186
	v_med3_f32 v10, v4, s58, v237
	v_mul_f32_e32 v4, 0x3e000000, v187
	v_med3_f32 v11, v4, s58, v237
	v_mov_b32_e32 v4, v199
	v_cvt_pk_fp8_f32 v4, v5, v7
	v_mov_b32_e32 v5, v199
	v_cvt_pk_fp8_f32 v5, v10, v11
	v_mul_f32_e32 v7, 0x3e000000, v188
	v_cvt_pk_fp8_f32 v4, v8, v9 op_sel:[0,0,1]
	v_mul_f32_e32 v8, 0x3e000000, v177
	v_med3_f32 v10, v8, s58, v237
	v_mul_f32_e32 v8, 0x3e000000, v182
	v_med3_f32 v9, v8, s58, v237
	v_mul_f32_e32 v8, 0x3e000000, v183
	v_med3_f32 v11, v8, s58, v237
	v_mul_f32_e32 v8, 0x3e000000, v184
	v_med3_f32 v12, v8, s58, v237
	v_mul_f32_e32 v8, 0x3e000000, v185
	v_med3_f32 v13, v8, s58, v237
	v_mul_f32_e32 v8, 0x3e000000, v174
	v_med3_f32 v14, v8, s58, v237
	v_mul_f32_e32 v8, 0x3e000000, v175
	v_med3_f32 v15, v8, s58, v237
	v_mov_b32_e32 v8, v199
	v_cvt_pk_fp8_f32 v8, v9, v11
	v_mov_b32_e32 v9, v199
	v_cvt_pk_fp8_f32 v9, v14, v15
	v_med3_f32 v7, v7, s58, v237
	v_mul_f32_e32 v11, 0x3e000000, v176
	v_cvt_pk_fp8_f32 v5, v7, v6 op_sel:[0,0,1]
	v_add_u32_e32 v6, v221, v225
	v_med3_f32 v11, v11, s58, v237
	v_ashrrev_i32_e32 v7, 31, v6
	v_cvt_pk_fp8_f32 v8, v12, v13 op_sel:[0,0,1]
	v_cvt_pk_fp8_f32 v9, v11, v10 op_sel:[0,0,1]
	v_lshlrev_b64 v[6:7], 11, v[6:7]
	v_lshl_add_u64 v[6:7], v[2:3], 0, v[6:7]
	v_mov_b32_e32 v40, v4
	v_mov_b32_e32 v41, v5
	v_mov_b32_e32 v42, v8
	v_mov_b32_e32 v43, v9
	v_lshl_add_u64 v[48:49], v[6:7], 0, v[52:53]
	s_nop 1
	v_permlane16_swap_b32_e32 v40, v42
	v_permlane16_swap_b32_e32 v41, v43
	global_store_dwordx4 v[48:49], v[40:43], off
	s_or_b64 exec, exec, s[4:5]
	v_cmp_lt_i32_e32 vcc, v227, v224
	s_and_saveexec_b64 s[4:5], vcc
	s_cbranch_execz .LBB0_1480
.LBB0_1488:
	v_mul_f32_e32 v4, 0x3e000000, v173
	v_med3_f32 v6, v4, s58, v237
	v_mul_f32_e32 v4, 0x3e000000, v178
	v_med3_f32 v5, v4, s58, v237
	v_mul_f32_e32 v4, 0x3e000000, v179
	v_med3_f32 v7, v4, s58, v237
	v_mul_f32_e32 v4, 0x3e000000, v180
	v_med3_f32 v8, v4, s58, v237
	v_mul_f32_e32 v4, 0x3e000000, v181
	v_med3_f32 v9, v4, s58, v237
	v_mul_f32_e32 v4, 0x3e000000, v170
	v_med3_f32 v10, v4, s58, v237
	v_mul_f32_e32 v4, 0x3e000000, v171
	v_med3_f32 v11, v4, s58, v237
	v_mov_b32_e32 v4, v199
	v_cvt_pk_fp8_f32 v4, v5, v7
	v_mov_b32_e32 v5, v199
	v_cvt_pk_fp8_f32 v5, v10, v11
	v_mul_f32_e32 v7, 0x3e000000, v172
	v_cvt_pk_fp8_f32 v4, v8, v9 op_sel:[0,0,1]
	v_mul_f32_e32 v8, 0x3e000000, v161
	v_med3_f32 v10, v8, s58, v237
	v_mul_f32_e32 v8, 0x3e000000, v166
	v_med3_f32 v9, v8, s58, v237
	v_mul_f32_e32 v8, 0x3e000000, v167
	v_med3_f32 v11, v8, s58, v237
	v_mul_f32_e32 v8, 0x3e000000, v168
	v_med3_f32 v12, v8, s58, v237
	v_mul_f32_e32 v8, 0x3e000000, v169
	v_med3_f32 v13, v8, s58, v237
	v_mul_f32_e32 v8, 0x3e000000, v158
	v_med3_f32 v14, v8, s58, v237
	v_mul_f32_e32 v8, 0x3e000000, v159
	v_med3_f32 v15, v8, s58, v237
	v_mov_b32_e32 v8, v199
	v_cvt_pk_fp8_f32 v8, v9, v11
	v_mov_b32_e32 v9, v199
	v_cvt_pk_fp8_f32 v9, v14, v15
	v_med3_f32 v7, v7, s58, v237
	v_mul_f32_e32 v11, 0x3e000000, v160
	v_cvt_pk_fp8_f32 v5, v7, v6 op_sel:[0,0,1]
	v_add_u32_e32 v6, v221, v227
	v_med3_f32 v11, v11, s58, v237
	v_ashrrev_i32_e32 v7, 31, v6
	v_cvt_pk_fp8_f32 v8, v12, v13 op_sel:[0,0,1]
	v_cvt_pk_fp8_f32 v9, v11, v10 op_sel:[0,0,1]
	v_lshlrev_b64 v[6:7], 11, v[6:7]
	v_lshl_add_u64 v[6:7], v[2:3], 0, v[6:7]
	v_mov_b32_e32 v44, v4
	v_mov_b32_e32 v45, v5
	v_mov_b32_e32 v46, v8
	v_mov_b32_e32 v47, v9
	v_lshl_add_u64 v[50:51], v[6:7], 0, v[52:53]
	s_nop 1
	v_permlane16_swap_b32_e32 v44, v46
	v_permlane16_swap_b32_e32 v45, v47
	global_store_dwordx4 v[50:51], v[44:47], off
	s_or_b64 exec, exec, s[4:5]
	v_cmp_lt_i32_e32 vcc, v228, v224
	s_and_saveexec_b64 s[4:5], vcc
	s_cbranch_execz .LBB0_1481
.LBB0_1489:
	v_mul_f32_e32 v4, 0x3e000000, v157
	v_med3_f32 v6, v4, s58, v237
	v_mul_f32_e32 v4, 0x3e000000, v162
	v_med3_f32 v5, v4, s58, v237
	v_mul_f32_e32 v4, 0x3e000000, v163
	v_med3_f32 v7, v4, s58, v237
	v_mul_f32_e32 v4, 0x3e000000, v164
	v_med3_f32 v8, v4, s58, v237
	v_mul_f32_e32 v4, 0x3e000000, v165
	v_med3_f32 v9, v4, s58, v237
	v_mul_f32_e32 v4, 0x3e000000, v154
	v_med3_f32 v10, v4, s58, v237
	v_mul_f32_e32 v4, 0x3e000000, v155
	v_med3_f32 v11, v4, s58, v237
	v_mov_b32_e32 v4, v199
	v_cvt_pk_fp8_f32 v4, v5, v7
	v_mov_b32_e32 v5, v199
	v_cvt_pk_fp8_f32 v5, v10, v11
	v_mul_f32_e32 v7, 0x3e000000, v156
	v_cvt_pk_fp8_f32 v4, v8, v9 op_sel:[0,0,1]
	v_mul_f32_e32 v8, 0x3e000000, v145
	v_med3_f32 v10, v8, s58, v237
	v_mul_f32_e32 v8, 0x3e000000, v150
	v_med3_f32 v9, v8, s58, v237
	v_mul_f32_e32 v8, 0x3e000000, v151
	v_med3_f32 v11, v8, s58, v237
	v_mul_f32_e32 v8, 0x3e000000, v152
	v_med3_f32 v12, v8, s58, v237
	v_mul_f32_e32 v8, 0x3e000000, v153
	v_med3_f32 v13, v8, s58, v237
	v_mul_f32_e32 v8, 0x3e000000, v142
	v_med3_f32 v14, v8, s58, v237
	v_mul_f32_e32 v8, 0x3e000000, v143
	v_med3_f32 v15, v8, s58, v237
	v_mov_b32_e32 v8, v199
	v_cvt_pk_fp8_f32 v8, v9, v11
	v_mov_b32_e32 v9, v199
	v_cvt_pk_fp8_f32 v9, v14, v15
	v_med3_f32 v7, v7, s58, v237
	v_mul_f32_e32 v11, 0x3e000000, v144
	v_cvt_pk_fp8_f32 v5, v7, v6 op_sel:[0,0,1]
	v_add_u32_e32 v6, v221, v228
	v_med3_f32 v11, v11, s58, v237
	v_ashrrev_i32_e32 v7, 31, v6
	v_cvt_pk_fp8_f32 v8, v12, v13 op_sel:[0,0,1]
	v_cvt_pk_fp8_f32 v9, v11, v10 op_sel:[0,0,1]
	v_lshlrev_b64 v[6:7], 11, v[6:7]
	v_lshl_add_u64 v[6:7], v[2:3], 0, v[6:7]
	v_mov_b32_e32 v40, v4
	v_mov_b32_e32 v41, v5
	v_mov_b32_e32 v42, v8
	v_mov_b32_e32 v43, v9
	v_lshl_add_u64 v[48:49], v[6:7], 0, v[52:53]
	s_nop 1
	v_permlane16_swap_b32_e32 v40, v42
	v_permlane16_swap_b32_e32 v41, v43
	global_store_dwordx4 v[48:49], v[40:43], off
	s_or_b64 exec, exec, s[4:5]
	v_cmp_lt_i32_e32 vcc, v229, v224
	s_and_saveexec_b64 s[4:5], vcc
	s_cbranch_execz .LBB0_1482
.LBB0_1490:
	v_mul_f32_e32 v4, 0x3e000000, v141
	v_med3_f32 v6, v4, s58, v237
	v_mul_f32_e32 v4, 0x3e000000, v146
	v_med3_f32 v5, v4, s58, v237
	v_mul_f32_e32 v4, 0x3e000000, v147
	v_med3_f32 v7, v4, s58, v237
	v_mul_f32_e32 v4, 0x3e000000, v148
	v_med3_f32 v8, v4, s58, v237
	v_mul_f32_e32 v4, 0x3e000000, v149
	v_med3_f32 v9, v4, s58, v237
	v_mul_f32_e32 v4, 0x3e000000, v138
	v_med3_f32 v10, v4, s58, v237
	v_mul_f32_e32 v4, 0x3e000000, v139
	v_med3_f32 v11, v4, s58, v237
	v_mov_b32_e32 v4, v199
	v_cvt_pk_fp8_f32 v4, v5, v7
	v_mov_b32_e32 v5, v199
	v_cvt_pk_fp8_f32 v5, v10, v11
	v_mul_f32_e32 v7, 0x3e000000, v140
	v_cvt_pk_fp8_f32 v4, v8, v9 op_sel:[0,0,1]
	v_mul_f32_e32 v8, 0x3e000000, v133
	v_med3_f32 v10, v8, s58, v237
	v_mul_f32_e32 v8, 0x3e000000, v134
	v_med3_f32 v9, v8, s58, v237
	v_mul_f32_e32 v8, 0x3e000000, v135
	v_med3_f32 v11, v8, s58, v237
	v_mul_f32_e32 v8, 0x3e000000, v136
	v_med3_f32 v12, v8, s58, v237
	v_mul_f32_e32 v8, 0x3e000000, v137
	v_med3_f32 v13, v8, s58, v237
	v_mul_f32_e32 v8, 0x3e000000, v130
	v_med3_f32 v14, v8, s58, v237
	v_mul_f32_e32 v8, 0x3e000000, v131
	v_med3_f32 v15, v8, s58, v237
	v_mov_b32_e32 v8, v199
	v_cvt_pk_fp8_f32 v8, v9, v11
	v_mov_b32_e32 v9, v199
	v_cvt_pk_fp8_f32 v9, v14, v15
	v_med3_f32 v7, v7, s58, v237
	v_mul_f32_e32 v11, 0x3e000000, v132
	v_cvt_pk_fp8_f32 v5, v7, v6 op_sel:[0,0,1]
	v_add_u32_e32 v6, v221, v229
	v_med3_f32 v11, v11, s58, v237
	v_ashrrev_i32_e32 v7, 31, v6
	v_cvt_pk_fp8_f32 v8, v12, v13 op_sel:[0,0,1]
	v_cvt_pk_fp8_f32 v9, v11, v10 op_sel:[0,0,1]
	v_lshlrev_b64 v[6:7], 11, v[6:7]
	v_lshl_add_u64 v[6:7], v[2:3], 0, v[6:7]
	v_mov_b32_e32 v44, v4
	v_mov_b32_e32 v45, v5
	v_mov_b32_e32 v46, v8
	v_mov_b32_e32 v47, v9
	v_lshl_add_u64 v[50:51], v[6:7], 0, v[52:53]
	s_nop 1
	v_permlane16_swap_b32_e32 v44, v46
	v_permlane16_swap_b32_e32 v45, v47
	global_store_dwordx4 v[50:51], v[44:47], off
	s_or_b64 exec, exec, s[4:5]
	v_cmp_lt_i32_e32 vcc, v230, v224
	s_and_saveexec_b64 s[4:5], vcc
	s_cbranch_execz .LBB0_1483
.LBB0_1491:
	v_mul_f32_e32 v4, 0x3e000000, v125
	v_med3_f32 v6, v4, s58, v237
	v_mul_f32_e32 v4, 0x3e000000, v126
	v_med3_f32 v5, v4, s58, v237
	v_mul_f32_e32 v4, 0x3e000000, v127
	v_med3_f32 v7, v4, s58, v237
	v_mul_f32_e32 v4, 0x3e000000, v128
	v_med3_f32 v8, v4, s58, v237
	v_mul_f32_e32 v4, 0x3e000000, v129
	v_med3_f32 v9, v4, s58, v237
	v_mul_f32_e32 v4, 0x3e000000, v122
	v_med3_f32 v10, v4, s58, v237
	v_mul_f32_e32 v4, 0x3e000000, v123
	v_med3_f32 v11, v4, s58, v237
	v_mov_b32_e32 v4, v199
	v_cvt_pk_fp8_f32 v4, v5, v7
	v_mov_b32_e32 v5, v199
	v_cvt_pk_fp8_f32 v5, v10, v11
	v_mul_f32_e32 v7, 0x3e000000, v124
	v_cvt_pk_fp8_f32 v4, v8, v9 op_sel:[0,0,1]
	v_mul_f32_e32 v8, 0x3e000000, v113
	v_med3_f32 v10, v8, s58, v237
	v_mul_f32_e32 v8, 0x3e000000, v118
	v_med3_f32 v9, v8, s58, v237
	v_mul_f32_e32 v8, 0x3e000000, v119
	v_med3_f32 v11, v8, s58, v237
	v_mul_f32_e32 v8, 0x3e000000, v120
	v_med3_f32 v12, v8, s58, v237
	v_mul_f32_e32 v8, 0x3e000000, v121
	v_med3_f32 v13, v8, s58, v237
	v_mul_f32_e32 v8, 0x3e000000, v110
	v_med3_f32 v14, v8, s58, v237
	v_mul_f32_e32 v8, 0x3e000000, v111
	v_med3_f32 v15, v8, s58, v237
	v_mov_b32_e32 v8, v199
	v_cvt_pk_fp8_f32 v8, v9, v11
	v_mov_b32_e32 v9, v199
	v_cvt_pk_fp8_f32 v9, v14, v15
	v_med3_f32 v7, v7, s58, v237
	v_mul_f32_e32 v11, 0x3e000000, v112
	v_cvt_pk_fp8_f32 v5, v7, v6 op_sel:[0,0,1]
	v_add_u32_e32 v6, v221, v230
	v_med3_f32 v11, v11, s58, v237
	v_ashrrev_i32_e32 v7, 31, v6
	v_cvt_pk_fp8_f32 v8, v12, v13 op_sel:[0,0,1]
	v_cvt_pk_fp8_f32 v9, v11, v10 op_sel:[0,0,1]
	v_lshlrev_b64 v[6:7], 11, v[6:7]
	v_lshl_add_u64 v[6:7], v[2:3], 0, v[6:7]
	v_mov_b32_e32 v40, v4
	v_mov_b32_e32 v41, v5
	v_mov_b32_e32 v42, v8
	v_mov_b32_e32 v43, v9
	v_lshl_add_u64 v[48:49], v[6:7], 0, v[52:53]
	s_nop 1
	v_permlane16_swap_b32_e32 v40, v42
	v_permlane16_swap_b32_e32 v41, v43
	global_store_dwordx4 v[48:49], v[40:43], off
	s_or_b64 exec, exec, s[4:5]
	v_cmp_lt_i32_e32 vcc, v231, v224
	s_and_saveexec_b64 s[4:5], vcc
	s_cbranch_execz .LBB0_1484
.LBB0_1492:
	v_mul_f32_e32 v4, 0x3e000000, v109
	v_med3_f32 v6, v4, s58, v237
	v_mul_f32_e32 v4, 0x3e000000, v114
	v_med3_f32 v5, v4, s58, v237
	v_mul_f32_e32 v4, 0x3e000000, v115
	v_med3_f32 v7, v4, s58, v237
	v_mul_f32_e32 v4, 0x3e000000, v116
	v_med3_f32 v8, v4, s58, v237
	v_mul_f32_e32 v4, 0x3e000000, v117
	v_med3_f32 v9, v4, s58, v237
	v_mul_f32_e32 v4, 0x3e000000, v106
	v_med3_f32 v10, v4, s58, v237
	v_mul_f32_e32 v4, 0x3e000000, v107
	v_med3_f32 v11, v4, s58, v237
	v_mov_b32_e32 v4, v199
	v_cvt_pk_fp8_f32 v4, v5, v7
	v_mov_b32_e32 v5, v199
	v_cvt_pk_fp8_f32 v5, v10, v11
	v_mul_f32_e32 v7, 0x3e000000, v108
	v_cvt_pk_fp8_f32 v4, v8, v9 op_sel:[0,0,1]
	v_mul_f32_e32 v8, 0x3e000000, v97
	v_med3_f32 v10, v8, s58, v237
	v_mul_f32_e32 v8, 0x3e000000, v102
	v_med3_f32 v9, v8, s58, v237
	v_mul_f32_e32 v8, 0x3e000000, v103
	v_med3_f32 v11, v8, s58, v237
	v_mul_f32_e32 v8, 0x3e000000, v104
	v_med3_f32 v12, v8, s58, v237
	v_mul_f32_e32 v8, 0x3e000000, v105
	v_med3_f32 v13, v8, s58, v237
	v_mul_f32_e32 v8, 0x3e000000, v94
	v_med3_f32 v14, v8, s58, v237
	v_mul_f32_e32 v8, 0x3e000000, v95
	v_med3_f32 v15, v8, s58, v237
	v_mov_b32_e32 v8, v199
	v_cvt_pk_fp8_f32 v8, v9, v11
	v_mov_b32_e32 v9, v199
	v_cvt_pk_fp8_f32 v9, v14, v15
	v_med3_f32 v7, v7, s58, v237
	v_mul_f32_e32 v11, 0x3e000000, v96
	v_cvt_pk_fp8_f32 v5, v7, v6 op_sel:[0,0,1]
	v_add_u32_e32 v6, v221, v231
	v_med3_f32 v11, v11, s58, v237
	v_ashrrev_i32_e32 v7, 31, v6
	v_cvt_pk_fp8_f32 v8, v12, v13 op_sel:[0,0,1]
	v_cvt_pk_fp8_f32 v9, v11, v10 op_sel:[0,0,1]
	v_lshlrev_b64 v[6:7], 11, v[6:7]
	v_lshl_add_u64 v[6:7], v[2:3], 0, v[6:7]
	v_mov_b32_e32 v44, v4
	v_mov_b32_e32 v45, v5
	v_mov_b32_e32 v46, v8
	v_mov_b32_e32 v47, v9
	v_lshl_add_u64 v[50:51], v[6:7], 0, v[52:53]
	s_nop 1
	v_permlane16_swap_b32_e32 v44, v46
	v_permlane16_swap_b32_e32 v45, v47
	global_store_dwordx4 v[50:51], v[44:47], off
	s_or_b64 exec, exec, s[4:5]
	v_cmp_lt_i32_e32 vcc, v232, v224
	s_and_saveexec_b64 s[4:5], vcc
	s_cbranch_execz .LBB0_1485
.LBB0_1493:
	v_mul_f32_e32 v4, 0x3e000000, v93
	v_med3_f32 v6, v4, s58, v237
	v_mul_f32_e32 v4, 0x3e000000, v98
	v_med3_f32 v5, v4, s58, v237
	v_mul_f32_e32 v4, 0x3e000000, v99
	v_med3_f32 v7, v4, s58, v237
	v_mul_f32_e32 v4, 0x3e000000, v100
	v_med3_f32 v8, v4, s58, v237
	v_mul_f32_e32 v4, 0x3e000000, v101
	v_med3_f32 v9, v4, s58, v237
	v_mul_f32_e32 v4, 0x3e000000, v90
	v_med3_f32 v10, v4, s58, v237
	v_mul_f32_e32 v4, 0x3e000000, v91
	v_med3_f32 v11, v4, s58, v237
	v_mov_b32_e32 v4, v199
	v_cvt_pk_fp8_f32 v4, v5, v7
	v_mov_b32_e32 v5, v199
	v_cvt_pk_fp8_f32 v5, v10, v11
	v_mul_f32_e32 v7, 0x3e000000, v92
	v_cvt_pk_fp8_f32 v4, v8, v9 op_sel:[0,0,1]
	v_mul_f32_e32 v8, 0x3e000000, v81
	v_med3_f32 v10, v8, s58, v237
	v_mul_f32_e32 v8, 0x3e000000, v86
	v_med3_f32 v9, v8, s58, v237
	v_mul_f32_e32 v8, 0x3e000000, v87
	v_med3_f32 v11, v8, s58, v237
	v_mul_f32_e32 v8, 0x3e000000, v88
	v_med3_f32 v12, v8, s58, v237
	v_mul_f32_e32 v8, 0x3e000000, v89
	v_med3_f32 v13, v8, s58, v237
	v_mul_f32_e32 v8, 0x3e000000, v78
	v_med3_f32 v14, v8, s58, v237
	v_mul_f32_e32 v8, 0x3e000000, v79
	v_med3_f32 v15, v8, s58, v237
	v_mov_b32_e32 v8, v199
	v_cvt_pk_fp8_f32 v8, v9, v11
	v_mov_b32_e32 v9, v199
	v_cvt_pk_fp8_f32 v9, v14, v15
	v_med3_f32 v7, v7, s58, v237
	v_mul_f32_e32 v11, 0x3e000000, v80
	v_cvt_pk_fp8_f32 v5, v7, v6 op_sel:[0,0,1]
	v_add_u32_e32 v6, v221, v232
	v_med3_f32 v11, v11, s58, v237
	v_ashrrev_i32_e32 v7, 31, v6
	v_cvt_pk_fp8_f32 v8, v12, v13 op_sel:[0,0,1]
	v_cvt_pk_fp8_f32 v9, v11, v10 op_sel:[0,0,1]
	v_lshlrev_b64 v[6:7], 11, v[6:7]
	v_lshl_add_u64 v[6:7], v[2:3], 0, v[6:7]
	v_mov_b32_e32 v40, v4
	v_mov_b32_e32 v41, v5
	v_mov_b32_e32 v42, v8
	v_mov_b32_e32 v43, v9
	v_lshl_add_u64 v[48:49], v[6:7], 0, v[52:53]
	s_nop 1
	v_permlane16_swap_b32_e32 v40, v42
	v_permlane16_swap_b32_e32 v41, v43
	global_store_dwordx4 v[48:49], v[40:43], off
	s_or_b64 exec, exec, s[4:5]
	v_cmp_lt_i32_e32 vcc, v233, v224
	s_and_saveexec_b64 s[4:5], vcc
	s_cbranch_execz .LBB0_1486
.LBB0_1494:
	v_mul_f32_e32 v4, 0x3e000000, v77
	v_med3_f32 v6, v4, s58, v237
	v_mul_f32_e32 v4, 0x3e000000, v82
	v_med3_f32 v5, v4, s58, v237
	v_mul_f32_e32 v4, 0x3e000000, v83
	v_med3_f32 v7, v4, s58, v237
	v_mul_f32_e32 v4, 0x3e000000, v84
	v_med3_f32 v8, v4, s58, v237
	v_mul_f32_e32 v4, 0x3e000000, v85
	v_med3_f32 v9, v4, s58, v237
	v_mul_f32_e32 v4, 0x3e000000, v74
	v_med3_f32 v10, v4, s58, v237
	v_mul_f32_e32 v4, 0x3e000000, v75
	v_med3_f32 v11, v4, s58, v237
	v_mov_b32_e32 v4, v199
	v_cvt_pk_fp8_f32 v4, v5, v7
	v_mov_b32_e32 v5, v199
	v_cvt_pk_fp8_f32 v5, v10, v11
	v_mul_f32_e32 v7, 0x3e000000, v76
	v_cvt_pk_fp8_f32 v4, v8, v9 op_sel:[0,0,1]
	v_mul_f32_e32 v8, 0x3e000000, v69
	v_med3_f32 v10, v8, s58, v237
	v_mul_f32_e32 v8, 0x3e000000, v70
	v_med3_f32 v9, v8, s58, v237
	v_mul_f32_e32 v8, 0x3e000000, v71
	v_med3_f32 v11, v8, s58, v237
	v_mul_f32_e32 v8, 0x3e000000, v72
	v_med3_f32 v12, v8, s58, v237
	v_mul_f32_e32 v8, 0x3e000000, v73
	v_med3_f32 v13, v8, s58, v237
	v_mul_f32_e32 v8, 0x3e000000, v66
	v_med3_f32 v14, v8, s58, v237
	v_mul_f32_e32 v8, 0x3e000000, v67
	v_med3_f32 v15, v8, s58, v237
	v_mov_b32_e32 v8, v199
	v_cvt_pk_fp8_f32 v8, v9, v11
	v_mov_b32_e32 v9, v199
	v_cvt_pk_fp8_f32 v9, v14, v15
	v_med3_f32 v7, v7, s58, v237
	v_mul_f32_e32 v11, 0x3e000000, v68
	v_cvt_pk_fp8_f32 v5, v7, v6 op_sel:[0,0,1]
	v_add_u32_e32 v6, v221, v233
	v_med3_f32 v11, v11, s58, v237
	v_ashrrev_i32_e32 v7, 31, v6
	v_cvt_pk_fp8_f32 v8, v12, v13 op_sel:[0,0,1]
	v_cvt_pk_fp8_f32 v9, v11, v10 op_sel:[0,0,1]
	v_lshlrev_b64 v[6:7], 11, v[6:7]
	v_lshl_add_u64 v[2:3], v[2:3], 0, v[6:7]
	v_mov_b32_e32 v44, v4
	v_mov_b32_e32 v45, v5
	v_mov_b32_e32 v46, v8
	v_mov_b32_e32 v47, v9
	v_lshl_add_u64 v[50:51], v[2:3], 0, v[52:53]
	s_nop 1
	v_permlane16_swap_b32_e32 v44, v46
	v_permlane16_swap_b32_e32 v45, v47
	global_store_dwordx4 v[50:51], v[44:47], off
	s_or_b64 exec, exec, s[4:5]
	s_and_b64 vcc, exec, s[0:1]
	s_mov_b64 s[0:1], -1
	s_cbranch_vccnz .LBB0_1466
